# NSA compressed branch: pass 1 reuses the tiles pass 0 left in the LDS ring when the branch has <=3 tiles (no second LDS-DMA); on top of router loop rewrite
# baseline (speedup 1.0000x reference)
; #define NSA_ISSUE(slot, Ksrc, Vsrc, loff) do { unsigned lo_ = (loff); asm volatile("" : "+v"(lo_));     \
;         NSA_GLDS((const char*)(Ksrc) + lo_, (unsigned)__builtin_amdgcn_readfirstlane(ldsb + L_K + (slot) * TB)); \
;         NSA_GLDS((const char*)(Vsrc) + lo_, (unsigned)__builtin_amdgcn_readfirstlane(ldsb + L_V + (slot) * TB)); } while (0)
; #define NSA_WAIT_BAR(n) asm volatile("s_waitcnt vmcnt(" #n ") lgkmcnt(0)\n\ts_barrier" ::: "memory")
; __device__ __forceinline__ void nsa_mfma_phase(Frame& F, int l, bf16* YC, int ypitch) {
;     ...
;         for (int pass = 0; pass < 2; ++pass) {
;             NSA_ISSUE(0, ckb, cvb, loffC);
;             if (ntc > 1) NSA_ISSUE(1, ckb + 64 * 64, cvb + 64 * 64, loffC);
;             for (int tt = 0; tt < ntc; ++tt) {
;                 if (tt + 1 < ntc) NSA_WAIT_BAR(2); else NSA_WAIT_BAR(0);
;                 if (tt + 2 < ntc) NSA_ISSUE((tt + 2) % 3, ckb + (size_t)(tt + 2) * 64 * 64, cvb + (size_t)(tt + 2) * 64 * 64, loffC);
.LBB0_484:
	v_mov_b32_e32 v0, v126
	s_cmp_eq_u64 s[60:61], 0
	s_cselect_b32 s100, 1, 0
	s_cmp_le_u32 s88, 3
	s_cselect_b32 s101, 1, 0
	s_and_b32 s100, s100, s101
	s_cbranch_scc1 .LBB0_486
	s_and_b64 vcc, exec, s[10:11]
	v_lshl_add_u64 v[34:35], s[0:1], 0, v[0:1]
	s_mov_b32 s5, m0
	s_mov_b32 m0, s49
	s_nop 0
	global_load_lds_dwordx4 v[34:35], off
	s_mov_b32 m0, s5
	v_lshl_add_u64 v[34:35], s[2:3], 0, v[0:1]
	s_mov_b32 s5, m0
	s_mov_b32 m0, s40
	s_nop 0
	global_load_lds_dwordx4 v[34:35], off
	s_mov_b32 m0, s5
	s_cbranch_vccz .LBB0_486
	v_mov_b32_e32 v0, v126
	s_add_i32 s5, s49, 0x2000
	v_lshl_add_u64 v[34:35], s[12:13], 0, v[0:1]
	s_mov_b32 s8, m0
	s_mov_b32 m0, s5
	s_nop 0
	global_load_lds_dwordx4 v[34:35], off
	s_mov_b32 m0, s8
	v_lshl_add_u64 v[34:35], s[44:45], 0, v[0:1]
	s_add_i32 s5, s49, 0x8000
	s_mov_b32 s8, m0
	s_mov_b32 m0, s5
	s_nop 0
	global_load_lds_dwordx4 v[34:35], off
	s_mov_b32 m0, s8

; #define NSA_ISSUE(slot, Ksrc, Vsrc, loff) do { unsigned lo_ = (loff); asm volatile("" : "+v"(lo_));     \
;         NSA_GLDS((const char*)(Ksrc) + lo_, (unsigned)__builtin_amdgcn_readfirstlane(ldsb + L_K + (slot) * TB)); \
;         NSA_GLDS((const char*)(Vsrc) + lo_, (unsigned)__builtin_amdgcn_readfirstlane(ldsb + L_V + (slot) * TB)); } while (0)
; #define NSA_WAIT_BAR(n) asm volatile("s_waitcnt vmcnt(" #n ") lgkmcnt(0)\n\ts_barrier" ::: "memory")
; __device__ __forceinline__ void nsa_mfma_phase(Frame& F, int l, bf16* YC, int ypitch) {
;     ...
;                 if (tt + 1 < ntc) NSA_WAIT_BAR(2); else NSA_WAIT_BAR(0);
;                 if (tt + 2 < ntc) NSA_ISSUE((tt + 2) % 3, ckb + (size_t)(tt + 2) * 64 * 64, cvb + (size_t)(tt + 2) * 64 * 64, loffC);
.LBB0_492:
	s_cmp_lg_u32 s100, 0
	s_cbranch_scc1 .LBB0_493
	s_mul_hi_u32 s9, s16, 0xaaaaaaab
	s_lshr_b32 s9, s9, 1
	s_mulk_i32 s9, 0x6000
	s_sub_i32 s9, s49, s9
	s_add_u32 s66, s28, s64
	v_mov_b32_e32 v0, v126
	s_addc_u32 s67, s29, s65
	s_add_i32 s9, s47, s9
	v_lshl_add_u64 v[34:35], s[66:67], 0, v[0:1]
	s_mov_b64 s[66:67], 0x804000
	v_lshl_add_u64 v[36:37], v[34:35], 0, s[66:67]
	s_add_i32 s43, s9, 0x4000
	s_mov_b32 s66, m0
	s_mov_b32 m0, s43
	s_nop 0
	global_load_lds_dwordx4 v[36:37], off
	s_mov_b32 m0, s66
	s_mov_b64 s[66:67], 0x884000
	v_lshl_add_u64 v[34:35], v[34:35], 0, s[66:67]
	s_add_i32 s9, s9, 0xa000
	s_mov_b32 s43, m0
	s_mov_b32 m0, s9
	s_nop 0
	global_load_lds_dwordx4 v[34:35], off
	s_mov_b32 m0, s43
